# baseline (speedup 1.0000x reference)
.LBB2_9:
	s_waitcnt lgkmcnt(12)
	v_mfma_f32_32x32x16_f16 v[16:31], v[140:143], v[172:175], v[16:31]
	v_exp_f32_e32 v99, v99
	v_exp_f32_e32 v100, v100
	v_exp_f32_e32 v101, v101
	v_add_u32_e32 v60, s29, v190
	ds_read_b128 v[56:59], v60
	ds_read_b128 v[176:179], v60 offset:512
	s_waitcnt lgkmcnt(12)
	v_mfma_f32_32x32x16_f16 v[0:15], v[136:139], v[64:67], v[0:15]
	v_exp_f32_e32 v102, v102
	v_exp_f32_e32 v103, v103
	v_exp_f32_e32 v104, v104
	ds_read_b128 v[172:175], v60 offset:2048
	ds_read_b128 v[168:171], v60 offset:2560
	s_waitcnt lgkmcnt(12)
	v_mfma_f32_32x32x16_f16 v[16:31], v[136:139], v[68:71], v[16:31]
	v_exp_f32_e32 v105, v105
	v_exp_f32_e32 v106, v106
	v_exp_f32_e32 v107, v107
	ds_read_b128 v[164:167], v60 offset:4096
	ds_read_b128 v[160:163], v60 offset:4608
	s_waitcnt lgkmcnt(12)
	v_mfma_f32_32x32x16_f16 v[0:15], v[132:135], v[76:79], v[0:15]
	v_exp_f32_e32 v108, v108
	v_exp_f32_e32 v109, v109
	v_exp_f32_e32 v110, v110
	ds_read_b128 v[156:159], v60 offset:6144
	ds_read_b128 v[152:155], v60 offset:6656
	s_waitcnt lgkmcnt(12)
	v_mfma_f32_32x32x16_f16 v[16:31], v[132:135], v[48:51], v[16:31]
	v_exp_f32_e32 v111, v111
	v_exp_f32_e32 v80, v80
	v_exp_f32_e32 v81, v81
	s_waitcnt vmcnt(2) lgkmcnt(0)
	s_barrier
	v_mfma_f32_32x32x16_f16 v[0:15], v[128:131], v[72:75], v[0:15]
	v_exp_f32_e32 v82, v82
	v_exp_f32_e32 v83, v83
	v_exp_f32_e32 v84, v84
	s_waitcnt lgkmcnt(8)
	v_mfma_f32_32x32x16_f16 v[16:31], v[128:131], v[52:55], v[16:31]
	v_exp_f32_e32 v85, v85
	v_exp_f32_e32 v86, v86
	v_exp_f32_e32 v87, v87
	s_andn2_b64 vcc, exec, s[8:9]
	s_cbranch_vccnz .LBB2_11
	v_add_u32_e32 v64, s23, v184
	ds_read_b128 v[48:51], v64 offset:49248
	ds_read_b128 v[52:55], v64 offset:49216
	ds_read_b128 v[60:63], v64 offset:49184
	ds_read_b128 v[64:67], v64 offset:49152
	s_waitcnt lgkmcnt(3)
	v_pk_mul_f32 v[12:13], v[12:13], v[48:49]
	s_waitcnt lgkmcnt(2)
	v_pk_mul_f32 v[8:9], v[8:9], v[52:53]
	s_waitcnt lgkmcnt(1)
	v_pk_mul_f32 v[4:5], v[4:5], v[60:61]
	v_pk_mul_f32 v[14:15], v[14:15], v[50:51]
	v_pk_mul_f32 v[10:11], v[10:11], v[54:55]
	v_pk_mul_f32 v[6:7], v[6:7], v[62:63]
	s_waitcnt lgkmcnt(0)
	v_pk_mul_f32 v[2:3], v[2:3], v[66:67]
	v_pk_mul_f32 v[0:1], v[0:1], v[64:65]
	v_pk_mul_f32 v[28:29], v[28:29], v[48:49]
	v_pk_mul_f32 v[24:25], v[24:25], v[52:53]
	v_pk_mul_f32 v[20:21], v[20:21], v[60:61]
	v_pk_mul_f32 v[30:31], v[30:31], v[50:51]
	v_pk_mul_f32 v[26:27], v[26:27], v[54:55]
	v_pk_mul_f32 v[22:23], v[22:23], v[62:63]
	v_pk_mul_f32 v[18:19], v[18:19], v[66:67]
	v_pk_mul_f32 v[16:17], v[16:17], v[64:65]

.LBB2_15:
	s_waitcnt lgkmcnt(12)
	v_mfma_f32_32x32x16_f16 v[16:31], v[140:143], v[144:147], v[16:31]
	v_exp_f32_e32 v67, v67
	v_exp_f32_e32 v68, v68
	v_exp_f32_e32 v69, v69
	v_add_u32_e32 v88, s33, v190
	ds_read_b128 v[172:175], v88
	ds_read_b128 v[168:171], v88 offset:512
	s_waitcnt lgkmcnt(12)
	v_mfma_f32_32x32x16_f16 v[0:15], v[136:139], v[96:99], v[0:15]
	v_exp_f32_e32 v70, v70
	v_exp_f32_e32 v71, v71
	v_exp_f32_e32 v72, v72
	ds_read_b128 v[164:167], v88 offset:2048
	ds_read_b128 v[160:163], v88 offset:2560
	s_waitcnt lgkmcnt(12)
	v_mfma_f32_32x32x16_f16 v[16:31], v[136:139], v[100:103], v[16:31]
	v_exp_f32_e32 v73, v73
	v_exp_f32_e32 v74, v74
	v_exp_f32_e32 v75, v75
	ds_read_b128 v[156:159], v88 offset:4096
	ds_read_b128 v[152:155], v88 offset:4608
	s_waitcnt lgkmcnt(12)
	v_mfma_f32_32x32x16_f16 v[0:15], v[132:135], v[104:107], v[0:15]
	v_exp_f32_e32 v76, v76
	v_exp_f32_e32 v77, v77
	v_exp_f32_e32 v78, v78
	ds_read_b128 v[148:151], v88 offset:6144
	ds_read_b128 v[144:147], v88 offset:6656
	s_waitcnt lgkmcnt(12)
	v_mfma_f32_32x32x16_f16 v[16:31], v[132:135], v[80:83], v[16:31]
	v_exp_f32_e32 v79, v79
	v_exp_f32_e32 v48, v48
	v_exp_f32_e32 v49, v49
	s_waitcnt vmcnt(2) lgkmcnt(0)
	s_barrier
	v_mfma_f32_32x32x16_f16 v[0:15], v[128:131], v[108:111], v[0:15]
	v_exp_f32_e32 v50, v50
	v_exp_f32_e32 v51, v51
	v_exp_f32_e32 v52, v52
	s_waitcnt lgkmcnt(8)
	v_mfma_f32_32x32x16_f16 v[16:31], v[128:131], v[84:87], v[16:31]
	v_exp_f32_e32 v53, v53
	v_exp_f32_e32 v54, v54
	v_exp_f32_e32 v55, v55
	s_andn2_b64 vcc, exec, s[8:9]
	s_cbranch_vccnz .LBB2_17
	v_add_u32_e32 v92, s23, v184
	ds_read_b128 v[80:83], v92 offset:49248
	ds_read_b128 v[84:87], v92 offset:49216
	ds_read_b128 v[88:91], v92 offset:49152
	ds_read_b128 v[92:95], v92 offset:49184
	s_waitcnt lgkmcnt(3)
	v_pk_mul_f32 v[14:15], v[14:15], v[82:83]
	v_pk_mul_f32 v[12:13], v[12:13], v[80:81]
	s_waitcnt lgkmcnt(2)
	v_pk_mul_f32 v[10:11], v[10:11], v[86:87]
	v_pk_mul_f32 v[8:9], v[8:9], v[84:85]
	s_waitcnt lgkmcnt(0)
	v_pk_mul_f32 v[6:7], v[6:7], v[94:95]
	v_pk_mul_f32 v[4:5], v[4:5], v[92:93]
	v_pk_mul_f32 v[2:3], v[2:3], v[90:91]
	v_pk_mul_f32 v[0:1], v[0:1], v[88:89]
	v_pk_mul_f32 v[30:31], v[30:31], v[82:83]
	v_pk_mul_f32 v[28:29], v[28:29], v[80:81]
	v_pk_mul_f32 v[26:27], v[26:27], v[86:87]
	v_pk_mul_f32 v[24:25], v[24:25], v[84:85]
	v_pk_mul_f32 v[22:23], v[22:23], v[94:95]
	v_pk_mul_f32 v[20:21], v[20:21], v[92:93]
	v_pk_mul_f32 v[18:19], v[18:19], v[90:91]
	v_pk_mul_f32 v[16:17], v[16:17], v[88:89]
